# baseline (speedup 1.0000x reference)
.LBB3_8:
	s_waitcnt lgkmcnt(0)
	s_nop 1
	s_nop 0
	v_mfma_f32_32x32x16_f16 v[80:95], a[192:195], a[128:131], 0
	s_nop 0
	v_mfma_f32_32x32x16_f16 v[48:63], a[192:195], a[160:163], 0
	s_nop 0
	v_mfma_f32_32x32x16_f16 v[64:79], a[224:227], a[128:131], 0
	s_nop 0
	v_mfma_f32_32x32x16_f16 v[32:47], a[224:227], a[160:163], 0
	s_nop 0
	v_mfma_f32_32x32x16_f16 v[80:95], a[196:199], a[132:135], v[80:95]
	s_nop 0
	v_mfma_f32_32x32x16_f16 v[48:63], a[196:199], a[164:167], v[48:63]
	s_nop 0
	v_mfma_f32_32x32x16_f16 v[64:79], a[228:231], a[132:135], v[64:79]
	s_nop 0
	v_mfma_f32_32x32x16_f16 v[32:47], a[228:231], a[164:167], v[32:47]
	s_nop 0
	v_mfma_f32_32x32x16_f16 v[80:95], a[200:203], a[136:139], v[80:95]
	s_nop 0
	v_mfma_f32_32x32x16_f16 v[48:63], a[200:203], a[168:171], v[48:63]
	s_nop 0
	v_mfma_f32_32x32x16_f16 v[64:79], a[232:235], a[136:139], v[64:79]
	s_nop 0
	v_mfma_f32_32x32x16_f16 v[32:47], a[232:235], a[168:171], v[32:47]
	s_nop 0
	v_mfma_f32_32x32x16_f16 v[80:95], a[204:207], a[140:143], v[80:95]
	s_nop 0
	v_mfma_f32_32x32x16_f16 v[48:63], a[204:207], a[172:175], v[48:63]
	s_nop 0
	v_mfma_f32_32x32x16_f16 v[64:79], a[236:239], a[140:143], v[64:79]
	s_nop 0
	v_mfma_f32_32x32x16_f16 v[32:47], a[236:239], a[172:175], v[32:47]
	s_nop 0
	v_mfma_f32_32x32x16_f16 v[80:95], a[208:211], a[144:147], v[80:95]
	s_mov_b32 s0, s33
	v_mfma_f32_32x32x16_f16 v[48:63], a[208:211], a[176:179], v[48:63]
	s_mov_b32 s1, s40
	v_mfma_f32_32x32x16_f16 v[64:79], a[240:243], a[144:147], v[64:79]
	s_mov_b32 s12, s41
	v_mfma_f32_32x32x16_f16 v[32:47], a[240:243], a[176:179], v[32:47]
	s_mov_b32 s13, s42
	v_mfma_f32_32x32x16_f16 v[80:95], a[212:215], a[148:151], v[80:95]
	s_mov_b32 s22, s43
	v_mfma_f32_32x32x16_f16 v[48:63], a[212:215], a[180:183], v[48:63]
	s_mov_b32 s23, s44
	v_mfma_f32_32x32x16_f16 v[64:79], a[244:247], a[148:151], v[64:79]
	s_mov_b32 s24, s45
	v_mfma_f32_32x32x16_f16 v[32:47], a[244:247], a[180:183], v[32:47]
	s_mov_b32 s30, s46
	v_mfma_f32_32x32x16_f16 v[80:95], a[216:219], a[152:155], v[80:95]
	s_mov_b32 s31, s47
	v_mfma_f32_32x32x16_f16 v[48:63], a[216:219], a[184:187], v[48:63]
	s_mov_b32 s34, s48
	v_mfma_f32_32x32x16_f16 v[64:79], a[248:251], a[152:155], v[64:79]
	s_mov_b32 s35, s49
	v_mfma_f32_32x32x16_f16 v[32:47], a[248:251], a[184:187], v[32:47]
	s_mov_b32 s91, s50
	v_mfma_f32_32x32x16_f16 v[80:95], a[220:223], a[156:159], v[80:95]
	s_mov_b32 s92, s51
	v_mfma_f32_32x32x16_f16 v[48:63], a[220:223], a[188:191], v[48:63]
	s_mov_b32 s93, s52
	v_mfma_f32_32x32x16_f16 v[64:79], a[252:255], a[156:159], v[64:79]
	s_mov_b32 s94, s53
	v_mfma_f32_32x32x16_f16 v[32:47], a[252:255], a[188:191], v[32:47]
	s_mov_b32 s95, s54
	s_nop 0
	s_nop 4
	s_waitcnt vmcnt(0) lgkmcnt(0)
	s_barrier
	s_nop 0
	s_mov_b32 m0, s0
	s_nop 0
	buffer_load_dwordx4 v211, s[16:19], s1 offen lds
	s_nop 0
	s_mov_b32 m0, s12
	s_nop 0
	buffer_load_dwordx4 v212, s[16:19], s13 offen lds
	ds_read_b128 a[192:195], v221 offset:0
	s_nop 0
	s_mov_b32 m0, s22
	s_nop 0
	buffer_load_dwordx4 v211, s[16:19], s23 offen lds
	ds_read_b128 a[196:199], v222 offset:0
	s_nop 0
	s_mov_b32 m0, s24
	s_nop 0
	buffer_load_dwordx4 v212, s[16:19], s30 offen lds
	ds_read_b128 a[200:203], v223 offset:0
	s_mov_b32 s22, s18
	s_mov_b32 s23, s19
	s_mov_b32 m0, s31
	s_nop 0
	buffer_load_dwordx4 v213, s[20:23], s34 offen lds
	ds_read_b128 a[204:207], v224 offset:0
	s_nop 0
	s_mov_b32 m0, s35
	s_nop 0
	buffer_load_dwordx4 v213, s[20:23], s91 offen lds
	ds_read_b128 a[208:211], v221 offset:128
	s_nop 0
	s_mov_b32 m0, s92
	s_nop 0
	buffer_load_dwordx4 v213, s[20:23], s93 offen lds
	ds_read_b128 a[212:215], v222 offset:128
	s_nop 0
	s_mov_b32 m0, s94
	s_nop 0
	buffer_load_dwordx4 v213, s[20:23], s95 offen lds
	ds_read_b128 a[216:219], v223 offset:128
	s_nop 0
	ds_read_b128 a[220:223], v224 offset:128
	v_max3_f32 v96, v80, v81, v64
	v_max3_f32 v97, v82, v83, v65
	s_nop 0
	v_max3_f32 v96, v96, v66, v67
	ds_read_b128 a[224:227], v221 offset:8192
	s_nop 0
	v_max3_f32 v96, v96, v84, v85
	v_max3_f32 v97, v97, v86, v87
	s_nop 0
	v_max3_f32 v96, v96, v68, v69
	v_max3_f32 v97, v97, v70, v71
	ds_read_b128 a[228:231], v222 offset:8192
	s_nop 0
	v_max3_f32 v96, v96, v88, v89
	v_max3_f32 v97, v97, v90, v91
	s_nop 0
	v_max3_f32 v96, v96, v72, v73
	v_max3_f32 v97, v97, v74, v75
	ds_read_b128 a[232:235], v223 offset:8192
	s_nop 0
	v_max3_f32 v96, v96, v92, v93
	v_max3_f32 v97, v97, v94, v95
	s_nop 0
	v_max3_f32 v96, v96, v76, v77
	v_max3_f32 v97, v97, v78, v79
	ds_read_b128 a[236:239], v224 offset:8192
	v_max3_f32 v98, v48, v49, v32
	v_max3_f32 v99, v50, v51, v33
	s_nop 0
	v_max3_f32 v98, v98, v34, v35
	ds_read_b128 a[240:243], v221 offset:8320
	s_nop 0
	v_max3_f32 v98, v98, v52, v53
	v_max3_f32 v99, v99, v54, v55
	s_nop 0
	v_max3_f32 v98, v98, v36, v37
	v_max3_f32 v99, v99, v38, v39
	ds_read_b128 a[244:247], v222 offset:8320
	s_nop 0
	v_max3_f32 v98, v98, v56, v57
	v_max3_f32 v99, v99, v58, v59
	s_nop 0
	v_max3_f32 v98, v98, v40, v41
	v_max3_f32 v99, v99, v42, v43
	ds_read_b128 a[248:251], v223 offset:8320
	s_nop 0
	v_max3_f32 v98, v98, v60, v61
	v_max3_f32 v99, v99, v62, v63
	s_nop 0
	v_max3_f32 v98, v98, v44, v45
	v_max3_f32 v99, v99, v46, v47
	ds_read_b128 a[252:255], v224 offset:8320
	v_max_f32_e32 v96, v96, v97
	s_nop 0
	v_mov_b32_e32 v97, v96
	s_nop 1
	v_permlane32_swap_b32_e32 v96, v97
	v_max_f32_e32 v229, v96, v97
	v_max_f32_e32 v96, v98, v99
	s_nop 0
	v_mov_b32_e32 v97, v96
	s_nop 1
	v_permlane32_swap_b32_e32 v96, v97
	v_max_f32_e32 v200, v96, v97
	v_sub_f32_e32 v128, v66, v229
	v_mbcnt_lo_u32_b32 v66, -1, 0
	v_mbcnt_hi_u32_b32 v66, -1, v66
	v_sub_f32_e32 v129, v67, v229
	v_xor_b32_e32 v67, 0x80000000, v229
	v_cmp_gt_u32_e32 vcc, 32, v66
	v_sub_f32_e32 v142, v32, v200
	v_mov_b32_e32 v230, 1.0
	v_sub_f32_e32 v143, v33, v200
	v_xor_b32_e32 v33, 0x80000000, v200
	v_cndmask_b32_e64 v66, 0, 1.0, vcc
	s_nop 1
	v_mfma_f32_32x32x2_f32 v[16:31], v66, v67, 0
	v_mbcnt_lo_u32_b32 v32, -1, 0
	v_mbcnt_hi_u32_b32 v32, -1, v32
	v_sub_f32_e32 v80, v80, v229
	v_sub_f32_e32 v81, v81, v229
	v_sub_f32_e32 v82, v82, v229
	v_sub_f32_e32 v83, v83, v229
	v_sub_f32_e32 v84, v84, v229
	v_sub_f32_e32 v85, v85, v229
	v_sub_f32_e32 v86, v86, v229
	v_sub_f32_e32 v87, v87, v229
	v_sub_f32_e32 v88, v88, v229
	v_sub_f32_e32 v89, v89, v229
	v_sub_f32_e32 v90, v90, v229
	v_sub_f32_e32 v91, v91, v229
	v_sub_f32_e32 v92, v92, v229
	v_sub_f32_e32 v93, v93, v229
	v_sub_f32_e32 v94, v94, v229
	v_sub_f32_e32 v95, v95, v229
	v_sub_f32_e32 v64, v64, v229
	v_sub_f32_e32 v65, v65, v229
	v_sub_f32_e32 v130, v68, v229
	s_nop 0
	v_cmp_gt_u32_e32 vcc, 32, v32
	v_sub_f32_e32 v131, v69, v229
	v_sub_f32_e32 v132, v70, v229
	v_sub_f32_e32 v133, v71, v229
	v_sub_f32_e32 v134, v72, v229
	v_sub_f32_e32 v135, v73, v229
	v_sub_f32_e32 v136, v74, v229
	v_sub_f32_e32 v137, v75, v229
	v_sub_f32_e32 v138, v76, v229
	v_sub_f32_e32 v139, v77, v229
	v_sub_f32_e32 v140, v78, v229
	v_sub_f32_e32 v141, v79, v229
	v_sub_f32_e32 v48, v48, v200
	v_sub_f32_e32 v49, v49, v200
	v_sub_f32_e32 v50, v50, v200
	v_sub_f32_e32 v51, v51, v200
	v_sub_f32_e32 v52, v52, v200
	v_sub_f32_e32 v53, v53, v200
	v_sub_f32_e32 v54, v54, v200
	v_sub_f32_e32 v55, v55, v200
	s_nop 1
	v_cndmask_b32_e64 v32, 0, 1.0, vcc
	v_sub_f32_e32 v56, v56, v200
	v_sub_f32_e32 v57, v57, v200
	v_sub_f32_e32 v58, v58, v200
	v_sub_f32_e32 v59, v59, v200
	v_sub_f32_e32 v60, v60, v200
	v_sub_f32_e32 v61, v61, v200
	v_sub_f32_e32 v62, v62, v200
	v_sub_f32_e32 v63, v63, v200
	v_sub_f32_e32 v144, v34, v200
	v_sub_f32_e32 v145, v35, v200
	v_sub_f32_e32 v146, v36, v200
	v_sub_f32_e32 v147, v37, v200
	v_sub_f32_e32 v183, v38, v200
	v_sub_f32_e32 v192, v39, v200
	v_sub_f32_e32 v193, v40, v200
	v_sub_f32_e32 v194, v41, v200
	v_sub_f32_e32 v195, v42, v200
	v_sub_f32_e32 v196, v43, v200
	v_sub_f32_e32 v197, v44, v200
	v_sub_f32_e32 v199, v45, v200
	v_sub_f32_e32 v231, v46, v200
	v_sub_f32_e32 v233, v47, v200
	s_nop 1
	v_mfma_f32_32x32x2_f32 v[0:15], v32, v33, 0
	v_exp_f32_e32 v112, v80
	v_exp_f32_e32 v113, v81
	v_exp_f32_e32 v114, v82
	v_exp_f32_e32 v115, v83
	v_add_f32_e32 v32, v201, v112
	v_add_f32_e32 v33, v201, v113
	v_exp_f32_e32 v116, v84
	v_exp_f32_e32 v117, v85
	v_exp_f32_e32 v118, v86
	v_add_f32_e32 v32, v32, v114
	v_add_f32_e32 v33, v33, v115
	v_exp_f32_e32 v119, v87
	v_exp_f32_e32 v120, v88
	v_add_f32_e32 v32, v32, v116
	v_add_f32_e32 v33, v33, v117
	s_nop 0
	v_add_f32_e32 v32, v32, v118
	v_exp_f32_e32 v121, v89
	v_exp_f32_e32 v122, v90
	v_exp_f32_e32 v123, v91
	v_add_f32_e32 v33, v33, v119
	v_add_f32_e32 v32, v32, v120
	v_exp_f32_e32 v124, v92
	v_exp_f32_e32 v125, v93
	v_add_f32_e32 v33, v33, v121
	v_add_f32_e32 v32, v32, v122
	s_nop 0
	v_add_f32_e32 v33, v33, v123
	v_exp_f32_e32 v126, v94
	v_exp_f32_e32 v127, v95
	v_exp_f32_e32 v96, v48
	v_add_f32_e32 v32, v32, v124
	v_add_f32_e32 v33, v33, v125
	v_exp_f32_e32 v97, v49
	v_exp_f32_e32 v98, v50
	v_add_f32_e32 v234, v32, v126
	v_add_f32_e32 v235, v33, v127
	v_add_f32_e32 v32, v201, v96
	v_exp_f32_e32 v99, v51
	v_exp_f32_e32 v100, v52
	v_exp_f32_e32 v101, v53
	v_add_f32_e32 v33, v201, v97
	v_add_f32_e32 v32, v32, v98
	v_exp_f32_e32 v102, v54
	v_exp_f32_e32 v103, v55
	v_add_f32_e32 v33, v33, v99
	v_add_f32_e32 v32, v32, v100
	s_nop 0
	v_add_f32_e32 v33, v33, v101
	v_exp_f32_e32 v104, v56
	v_exp_f32_e32 v105, v57
	v_exp_f32_e32 v106, v58
	v_add_f32_e32 v32, v32, v102
	v_add_f32_e32 v33, v33, v103
	v_exp_f32_e32 v107, v59
	v_exp_f32_e32 v108, v60
	v_add_f32_e32 v32, v32, v104
	v_add_f32_e32 v33, v33, v105
	s_nop 0
	v_add_f32_e32 v32, v32, v106
	v_exp_f32_e32 v109, v61
	v_exp_f32_e32 v110, v62
	v_exp_f32_e32 v111, v63
	v_add_f32_e32 v33, v33, v107
	v_add_f32_e32 v32, v32, v108
	s_nop 0
	s_waitcnt lgkmcnt(0)
	v_add_f32_e32 v33, v33, v109
	v_add_f32_e32 v236, v32, v110
	s_nop 0
	v_add_f32_e32 v237, v33, v111
	v_mfma_f32_32x32x16_f16 v[80:95], a[192:195], a[128:131], v[16:31]
	ds_read_b64_tr_b16 v[168:169], v210 offset:0
	v_exp_f32_e32 v238, v64
	v_exp_f32_e32 v239, v65
	v_cvt_pk_f16_f32 v152, v112, v113
	v_exp_f32_e32 v112, v128
	v_exp_f32_e32 v113, v129
	v_mfma_f32_32x32x16_f16 v[64:79], a[192:195], a[160:163], v[0:15]
	ds_read_b64_tr_b16 v[170:171], v210 offset:0x800
	v_cvt_pk_f16_f32 v153, v114, v115
	v_exp_f32_e32 v114, v130
	v_exp_f32_e32 v115, v131
	v_mfma_f32_32x32x16_f16 v[48:63], a[224:227], a[128:131], v[16:31]
	ds_read_b64_tr_b16 v[172:173], v210 offset:0x200
	v_cvt_pk_f16_f32 v154, v116, v117
	v_mfma_f32_32x32x16_f16 v[32:47], a[224:227], a[160:163], v[0:15]
	ds_read_b64_tr_b16 v[174:175], v210 offset:0xa00
	ds_read_b64_tr_b16 v[164:165], v210 offset:0x400
	v_exp_f32_e32 v240, v132
	v_exp_f32_e32 v241, v133
	v_cvt_pk_f16_f32 v155, v118, v119
	v_exp_f32_e32 v184, v134
	v_exp_f32_e32 v185, v135
	v_mfma_f32_32x32x16_f16 v[80:95], a[196:199], a[132:135], v[80:95]
	ds_read_b64_tr_b16 v[166:167], v210 offset:0xc00
	v_cvt_pk_f16_f32 v128, v120, v121
	v_exp_f32_e32 v186, v136
	v_exp_f32_e32 v187, v137
	v_mfma_f32_32x32x16_f16 v[64:79], a[196:199], a[164:167], v[64:79]
	ds_read_b64_tr_b16 v[176:177], v210 offset:0x600
	v_cvt_pk_f16_f32 v129, v122, v123
	v_exp_f32_e32 v188, v138
	v_exp_f32_e32 v189, v139
	v_mfma_f32_32x32x16_f16 v[48:63], a[228:231], a[132:135], v[48:63]
	ds_read_b64_tr_b16 v[178:179], v210 offset:0xe00
	v_cvt_pk_f16_f32 v130, v124, v125
	v_mfma_f32_32x32x16_f16 v[32:47], a[228:231], a[164:167], v[32:47]
	ds_read_b64_tr_b16 v[160:161], v210 offset:0x1000
	v_exp_f32_e32 v190, v140
	v_exp_f32_e32 v191, v141
	ds_read_b64_tr_b16 v[162:163], v210 offset:0x1800
	v_cvt_pk_f16_f32 v131, v126, v127
	v_exp_f32_e32 v141, v142
	v_exp_f32_e32 v142, v143
	v_mfma_f32_32x32x16_f16 v[80:95], a[200:203], a[136:139], v[80:95]
	ds_read_b64_tr_b16 v[156:157], v210 offset:0x1200
	v_cvt_pk_f16_f32 v180, v96, v97
	v_exp_f32_e32 v143, v144
	v_mfma_f32_32x32x16_f16 v[64:79], a[200:203], a[168:171], v[64:79]
	ds_read_b64_tr_b16 v[158:159], v210 offset:0x1a00
	v_exp_f32_e32 v242, v145
	v_cvt_pk_f16_f32 v181, v98, v99
	v_mfma_f32_32x32x16_f16 v[48:63], a[232:235], a[136:139], v[48:63]
	ds_read_b64_tr_b16 v[148:149], v210 offset:0x1400
	v_exp_f32_e32 v243, v146
	v_exp_f32_e32 v244, v147
	v_cvt_pk_f16_f32 v182, v100, v101
	v_mfma_f32_32x32x16_f16 v[32:47], a[232:235], a[168:171], v[32:47]
	ds_read_b64_tr_b16 v[150:151], v210 offset:0x1c00
	ds_read_b64_tr_b16 v[136:137], v210 offset:0x1600
	v_exp_f32_e32 v245, v183
	v_exp_f32_e32 v246, v192
	v_cvt_pk_f16_f32 v183, v102, v103
	v_exp_f32_e32 v192, v193
	v_exp_f32_e32 v193, v194
	v_mfma_f32_32x32x16_f16 v[80:95], a[204:207], a[140:143], v[80:95]
	ds_read_b64_tr_b16 v[138:139], v210 offset:0x1e00
	v_cvt_pk_f16_f32 v144, v104, v105
	v_exp_f32_e32 v194, v195
	v_exp_f32_e32 v195, v196
	v_mfma_f32_32x32x16_f16 v[64:79], a[204:207], a[172:175], v[64:79]
	ds_read_b64_tr_b16 v[132:133], v210 offset:0x2000
	v_cvt_pk_f16_f32 v145, v106, v107
	v_exp_f32_e32 v198, v197
	v_exp_f32_e32 v199, v199
	v_mfma_f32_32x32x16_f16 v[48:63], a[236:239], a[140:143], v[48:63]
	ds_read_b64_tr_b16 v[134:135], v210 offset:0x2800
	v_cvt_pk_f16_f32 v146, v108, v109
	v_mfma_f32_32x32x16_f16 v[32:47], a[236:239], a[172:175], v[32:47]
	ds_read_b64_tr_b16 v[124:125], v210 offset:0x2200
	v_exp_f32_e32 v232, v231
	v_exp_f32_e32 v233, v233
	ds_read_b64_tr_b16 v[126:127], v210 offset:0x2a00
	v_cvt_pk_f16_f32 v147, v110, v111
	s_mov_b32 s0, s55
	v_mfma_f32_32x32x16_f16 v[80:95], a[208:211], a[144:147], v[80:95]
	ds_read_b64_tr_b16 v[120:121], v210 offset:0x2400
	v_cvt_pk_f16_f32 v116, v238, v239
	v_add_f32_e32 v96, v234, v238
	v_add_f32_e32 v97, v235, v239
	s_mov_b32 s1, s56
	v_mfma_f32_32x32x16_f16 v[64:79], a[208:211], a[176:179], v[64:79]
	ds_read_b64_tr_b16 v[122:123], v210 offset:0x2c00
	v_cvt_pk_f16_f32 v117, v112, v113
	v_add_f32_e32 v96, v96, v112
	v_add_f32_e32 v97, v97, v113
	s_mov_b32 s12, s57
	v_mfma_f32_32x32x16_f16 v[48:63], a[240:243], a[144:147], v[48:63]
	ds_read_b64_tr_b16 v[112:113], v210 offset:0x2600
	v_cvt_pk_f16_f32 v118, v114, v115
	v_add_f32_e32 v96, v96, v114
	v_add_f32_e32 v97, v97, v115
	s_mov_b32 s13, s58
	v_mfma_f32_32x32x16_f16 v[32:47], a[240:243], a[176:179], v[32:47]
	ds_read_b64_tr_b16 v[114:115], v210 offset:0x2e00
	ds_read_b64_tr_b16 v[108:109], v210 offset:0x3000
	v_cvt_pk_f16_f32 v119, v240, v241
	v_add_f32_e32 v96, v96, v240
	v_add_f32_e32 v97, v97, v241
	s_mov_b32 s24, s59
	v_mfma_f32_32x32x16_f16 v[80:95], a[212:215], a[148:151], v[80:95]
	ds_read_b64_tr_b16 v[110:111], v210 offset:0x3800
	v_add_f32_e32 v96, v96, v184
	v_add_f32_e32 v97, v97, v185
	s_mov_b32 s30, s60
	v_mfma_f32_32x32x16_f16 v[64:79], a[212:215], a[180:183], v[64:79]
	ds_read_b64_tr_b16 v[104:105], v210 offset:0x3200
	v_add_f32_e32 v96, v96, v186
	v_add_f32_e32 v97, v97, v187
	s_mov_b32 s31, s61
	v_mfma_f32_32x32x16_f16 v[48:63], a[244:247], a[148:151], v[48:63]
	ds_read_b64_tr_b16 v[106:107], v210 offset:0x3a00
	v_add_f32_e32 v96, v96, v188
	v_add_f32_e32 v97, v97, v189
	s_mov_b32 s34, s62
	v_mfma_f32_32x32x16_f16 v[32:47], a[244:247], a[180:183], v[32:47]
	ds_read_b64_tr_b16 v[100:101], v210 offset:0x3400
	ds_read_b64_tr_b16 v[102:103], v210 offset:0x3c00
	v_add_f32_e32 v196, v96, v190
	v_add_f32_e32 v197, v97, v191
	s_mov_b32 s35, s38
	v_mfma_f32_32x32x16_f16 v[80:95], a[216:219], a[152:155], v[80:95]
	ds_read_b64_tr_b16 v[96:97], v210 offset:0x3600
	v_cvt_pk_f16_f32 v140, v141, v142
	v_add_f32_e32 v231, v236, v141
	v_add_f32_e32 v142, v237, v142
	s_mov_b32 s91, s40
	v_mfma_f32_32x32x16_f16 v[64:79], a[216:219], a[184:187], v[64:79]
	ds_read_b64_tr_b16 v[98:99], v210 offset:0x3e00
	v_cvt_pk_f16_f32 v141, v143, v242
	v_add_f32_e32 v143, v231, v143
	v_add_f32_e32 v231, v142, v242
	v_mfma_f32_32x32x16_f16 v[48:63], a[248:251], a[152:155], v[48:63]
	s_mov_b32 s92, s63
	v_cvt_pk_f16_f32 v142, v243, v244
	v_add_f32_e32 v234, v143, v243
	v_add_f32_e32 v231, v231, v244
	v_mfma_f32_32x32x16_f16 v[32:47], a[248:251], a[184:187], v[32:47]
	s_mov_b32 s93, s64
	v_cvt_pk_f16_f32 v143, v245, v246
	v_add_f32_e32 v234, v234, v245
	v_add_f32_e32 v231, v231, v246
	v_mfma_f32_32x32x16_f16 v[80:95], a[220:223], a[156:159], v[80:95]
	s_mov_b32 s94, s65
	v_add_f32_e32 v234, v234, v192
	v_add_f32_e32 v231, v231, v193
	v_mfma_f32_32x32x16_f16 v[64:79], a[220:223], a[188:191], v[64:79]
	s_mov_b32 s95, s44
	v_add_f32_e32 v234, v234, v194
	v_add_f32_e32 v231, v231, v195
	v_mfma_f32_32x32x16_f16 v[48:63], a[252:255], a[156:159], v[48:63]
	s_mov_b32 s96, s66
	v_add_f32_e32 v234, v234, v198
	v_add_f32_e32 v231, v231, v199
	v_mfma_f32_32x32x16_f16 v[32:47], a[252:255], a[188:191], v[32:47]
	s_mov_b32 s97, s67
	v_add_f32_e32 v234, v234, v232
	v_add_f32_e32 v231, v231, v233
	s_nop 0
	s_nop 4
	v_add_f32_e32 v196, v196, v197
	s_waitcnt vmcnt(0) lgkmcnt(0)
	s_barrier
	s_nop 0
	v_mov_b32_e32 v197, v196
	s_nop 1
	v_permlane32_swap_b32_e32 v196, v197
	v_add_f32_e32 v196, v196, v197
	s_nop 0
	v_add_f32_e32 v197, v201, v196
	v_add_f32_e32 v196, v234, v231
	s_nop 0
	v_mov_b32_e32 v231, v196
	s_nop 1
	v_permlane32_swap_b32_e32 v196, v231
	v_add_f32_e32 v196, v196, v231
	s_nop 0
	v_add_f32_e32 v196, v201, v196
	s_nop 1
	v_mfma_f32_32x32x16_f16 a[0:15], v[168:171], v[152:155], 0
	s_mov_b32 m0, s0
	s_nop 0
	buffer_load_dwordx4 v211, s[16:19], s1 offen lds
	s_nop 0
	v_mfma_f32_32x32x16_f16 a[16:31], v[168:171], v[180:183], 0
	s_mov_b32 m0, s12
	s_nop 0
	buffer_load_dwordx4 v212, s[16:19], s13 offen lds
	ds_read_b128 a[192:195], v206 offset:0
	s_nop 0
	v_mfma_f32_32x32x16_f16 a[32:47], v[172:175], v[152:155], 0
	s_mov_b32 m0, s24
	s_nop 0
	buffer_load_dwordx4 v211, s[16:19], s30 offen lds
	ds_read_b128 a[196:199], v207 offset:0
	s_nop 0
	v_mfma_f32_32x32x16_f16 a[48:63], v[172:175], v[180:183], 0
	s_mov_b32 m0, s31
	s_nop 0
	buffer_load_dwordx4 v212, s[16:19], s34 offen lds
	ds_read_b128 a[200:203], v208 offset:0
	s_nop 0
	v_mfma_f32_32x32x16_f16 a[64:79], v[164:167], v[152:155], 0
	s_mov_b32 m0, s35
	s_nop 0
	buffer_load_dwordx4 v213, s[20:23], s91 offen lds
	ds_read_b128 a[204:207], v209 offset:0
	s_nop 0
	v_mfma_f32_32x32x16_f16 a[80:95], v[164:167], v[180:183], 0
	s_mov_b32 m0, s92
	s_nop 0
	buffer_load_dwordx4 v213, s[20:23], s93 offen lds
	ds_read_b128 a[208:211], v206 offset:128
	s_nop 0
	v_mfma_f32_32x32x16_f16 a[96:111], v[176:179], v[152:155], 0
	s_mov_b32 m0, s94
	s_nop 0
	buffer_load_dwordx4 v213, s[20:23], s95 offen lds
	ds_read_b128 a[212:215], v207 offset:128
	s_nop 0
	v_mfma_f32_32x32x16_f16 a[112:127], v[176:179], v[180:183], 0
	s_mov_b32 m0, s96
	s_nop 0
	buffer_load_dwordx4 v213, s[20:23], s97 offen lds
	ds_read_b128 a[216:219], v208 offset:128
	s_nop 0
	v_mfma_f32_32x32x16_f16 a[0:15], v[160:163], v[128:131], a[0:15]
	ds_read_b128 a[220:223], v209 offset:128
	v_max3_f32 v152, v80, v81, v48
	v_max3_f32 v153, v82, v83, v49
	s_nop 0
	v_max3_f32 v152, v152, v50, v51
	v_mfma_f32_32x32x16_f16 a[16:31], v[160:163], v[144:147], a[16:31]
	ds_read_b128 a[224:227], v206 offset:8192
	s_nop 0
	v_max3_f32 v152, v152, v84, v85
	v_max3_f32 v153, v153, v86, v87
	s_nop 0
	v_max3_f32 v152, v152, v52, v53
	v_max3_f32 v153, v153, v54, v55
	v_mfma_f32_32x32x16_f16 a[32:47], v[156:159], v[128:131], a[32:47]
	ds_read_b128 a[228:231], v207 offset:8192
	s_nop 0
	v_max3_f32 v152, v152, v88, v89
	v_max3_f32 v153, v153, v90, v91
	s_nop 0
	v_max3_f32 v152, v152, v56, v57
	v_max3_f32 v153, v153, v58, v59
	v_mfma_f32_32x32x16_f16 a[48:63], v[156:159], v[144:147], a[48:63]
	ds_read_b128 a[232:235], v208 offset:8192
	s_nop 0
	v_max3_f32 v152, v152, v92, v93
	v_max3_f32 v153, v153, v94, v95
	s_nop 0
	v_max3_f32 v152, v152, v60, v61
	v_max3_f32 v153, v153, v62, v63
	v_mfma_f32_32x32x16_f16 a[64:79], v[148:151], v[128:131], a[64:79]
	ds_read_b128 a[236:239], v209 offset:8192
	v_max3_f32 v154, v64, v65, v32
	v_max3_f32 v155, v66, v67, v33
	s_nop 0
	v_max3_f32 v154, v154, v34, v35
	v_mfma_f32_32x32x16_f16 a[80:95], v[148:151], v[144:147], a[80:95]
	ds_read_b128 a[240:243], v206 offset:8320
	s_nop 0
	v_max3_f32 v148, v154, v68, v69
	v_max3_f32 v149, v155, v70, v71
	s_nop 0
	v_max3_f32 v148, v148, v36, v37
	v_max3_f32 v149, v149, v38, v39
	v_mfma_f32_32x32x16_f16 a[96:111], v[136:139], v[128:131], a[96:111]
	ds_read_b128 a[244:247], v207 offset:8320
	s_nop 0
	v_max3_f32 v128, v148, v72, v73
	v_max3_f32 v129, v149, v74, v75
	s_nop 0
	v_max3_f32 v128, v128, v40, v41
	v_max3_f32 v129, v129, v42, v43
	v_mfma_f32_32x32x16_f16 a[112:127], v[136:139], v[144:147], a[112:127]
	ds_read_b128 a[248:251], v208 offset:8320
	s_nop 0
	v_max3_f32 v128, v128, v76, v77
	v_max3_f32 v129, v129, v78, v79
	s_nop 0
	v_max3_f32 v128, v128, v44, v45
	v_max3_f32 v130, v129, v46, v47
	v_mfma_f32_32x32x16_f16 a[0:15], v[132:135], v[116:119], a[0:15]
	ds_read_b128 a[252:255], v209 offset:8320
	v_max_f32_e32 v129, v152, v153
	s_nop 0
	v_mov_b32_e32 v131, v129
	s_nop 1
	v_permlane32_swap_b32_e32 v129, v131
	v_max_f32_e32 v129, v129, v131
	v_mfma_f32_32x32x16_f16 a[16:31], v[132:135], v[140:143], a[16:31]
	v_max_f32_e32 v128, v128, v130
	s_nop 0
	v_mov_b32_e32 v130, v128
	s_nop 1
	v_permlane32_swap_b32_e32 v128, v130
	v_max_f32_e32 v128, v128, v130
	v_max_f32_e32 v130, v129, v128
	v_mfma_f32_32x32x16_f16 a[32:47], v[124:127], v[116:119], a[32:47]
	v_cmp_lt_f32_e32 vcc, s79, v130
	s_cmp_lg_u64 vcc, 0
	s_cselect_b64 s[0:1], -1, 0
	s_cbranch_vccnz .LBB3_26
	v_mov_b32_e32 v231, 1.0

.LBB3_12:
	v_exp_f32_e32 v48, v48
	v_exp_f32_e32 v49, v49
	v_mfma_f32_32x32x16_f16 v[112:127], a[192:195], a[128:131], v[16:31]
	ds_read_b64_tr_b16 v[180:181], v225 offset:0
	v_cvt_pk_f16_f32 v164, v128, v129
	v_exp_f32_e32 v50, v50
	v_exp_f32_e32 v51, v51
	v_mfma_f32_32x32x16_f16 v[96:111], a[192:195], a[160:163], v[0:15]
	ds_read_b64_tr_b16 v[182:183], v225 offset:0x800
	v_cvt_pk_f16_f32 v165, v130, v131
	v_mfma_f32_32x32x16_f16 v[80:95], a[224:227], a[128:131], v[16:31]
	ds_read_b64_tr_b16 v[184:185], v225 offset:0x200
	v_exp_f32_e32 v238, v52
	v_exp_f32_e32 v239, v53
	v_cvt_pk_f16_f32 v166, v132, v133
	v_mfma_f32_32x32x16_f16 v[64:79], a[224:227], a[160:163], v[0:15]
	ds_read_b64_tr_b16 v[186:187], v225 offset:0xa00
	ds_read_b64_tr_b16 v[176:177], v225 offset:0x400
	v_exp_f32_e32 v244, v54
	v_exp_f32_e32 v245, v55
	v_cvt_pk_f16_f32 v167, v134, v135
	v_exp_f32_e32 v198, v56
	v_exp_f32_e32 v199, v57
	v_mfma_f32_32x32x16_f16 v[112:127], a[196:199], a[132:135], v[112:127]
	ds_read_b64_tr_b16 v[178:179], v225 offset:0xc00
	v_cvt_pk_f16_f32 v128, v136, v137
	v_exp_f32_e32 v232, v58
	v_exp_f32_e32 v233, v59
	v_mfma_f32_32x32x16_f16 v[96:111], a[196:199], a[164:167], v[96:111]
	ds_read_b64_tr_b16 v[188:189], v225 offset:0x600
	v_cvt_pk_f16_f32 v129, v138, v139
	v_exp_f32_e32 v234, v60
	v_exp_f32_e32 v235, v61
	v_mfma_f32_32x32x16_f16 v[80:95], a[228:231], a[132:135], v[80:95]
	ds_read_b64_tr_b16 v[190:191], v225 offset:0xe00
	v_cvt_pk_f16_f32 v130, v140, v141
	v_mfma_f32_32x32x16_f16 v[64:79], a[228:231], a[164:167], v[64:79]
	ds_read_b64_tr_b16 v[172:173], v225 offset:0x1000
	v_exp_f32_e32 v236, v62
	v_exp_f32_e32 v237, v63
	ds_read_b64_tr_b16 v[174:175], v225 offset:0x1800
	v_cvt_pk_f16_f32 v131, v142, v143
	v_exp_f32_e32 v141, v32
	v_exp_f32_e32 v142, v33
	v_mfma_f32_32x32x16_f16 v[112:127], a[200:203], a[136:139], v[112:127]
	ds_read_b64_tr_b16 v[168:169], v225 offset:0x1200
	v_cvt_pk_f16_f32 v192, v144, v145
	v_exp_f32_e32 v143, v34
	v_mfma_f32_32x32x16_f16 v[96:111], a[200:203], a[168:171], v[96:111]
	ds_read_b64_tr_b16 v[170:171], v225 offset:0x1a00
	v_exp_f32_e32 v246, v35
	v_cvt_pk_f16_f32 v193, v146, v147
	v_mfma_f32_32x32x16_f16 v[80:95], a[232:235], a[136:139], v[80:95]
	ds_read_b64_tr_b16 v[160:161], v225 offset:0x1400
	v_exp_f32_e32 v247, v36
	v_exp_f32_e32 v248, v37
	v_cvt_pk_f16_f32 v194, v148, v149
	v_mfma_f32_32x32x16_f16 v[64:79], a[232:235], a[168:171], v[64:79]
	ds_read_b64_tr_b16 v[162:163], v225 offset:0x1c00
	ds_read_b64_tr_b16 v[136:137], v225 offset:0x1600
	v_exp_f32_e32 v249, v38
	v_exp_f32_e32 v250, v39
	v_cvt_pk_f16_f32 v195, v150, v151
	v_exp_f32_e32 v148, v40
	v_exp_f32_e32 v149, v41
	v_mfma_f32_32x32x16_f16 v[112:127], a[204:207], a[140:143], v[112:127]
	ds_read_b64_tr_b16 v[138:139], v225 offset:0x1e00
	v_cvt_pk_f16_f32 v144, v152, v153
	v_exp_f32_e32 v150, v42
	v_exp_f32_e32 v151, v43
	v_mfma_f32_32x32x16_f16 v[96:111], a[204:207], a[172:175], v[96:111]
	ds_read_b64_tr_b16 v[132:133], v225 offset:0x2000
	v_cvt_pk_f16_f32 v145, v154, v155
	v_exp_f32_e32 v152, v44
	v_exp_f32_e32 v153, v45
	v_mfma_f32_32x32x16_f16 v[80:95], a[236:239], a[140:143], v[80:95]
	ds_read_b64_tr_b16 v[134:135], v225 offset:0x2800
	v_cvt_pk_f16_f32 v146, v156, v157
	v_mfma_f32_32x32x16_f16 v[64:79], a[236:239], a[172:175], v[64:79]
	ds_read_b64_tr_b16 v[60:61], v225 offset:0x2200
	v_exp_f32_e32 v154, v46
	v_exp_f32_e32 v155, v47
	ds_read_b64_tr_b16 v[62:63], v225 offset:0x2a00
	v_cvt_pk_f16_f32 v147, v158, v159
	s_mov_b32 s0, s33
	v_mfma_f32_32x32x16_f16 v[112:127], a[208:211], a[144:147], v[112:127]
	ds_read_b64_tr_b16 v[56:57], v225 offset:0x2400
	v_cvt_pk_f16_f32 v52, v48, v49
	v_add_f32_e32 v32, v241, v48
	v_add_f32_e32 v33, v240, v49
	s_add_i32 s31, s36, s12
	s_add_i32 s24, s31, 0x10000
	s_mov_b32 s1, s24
	v_mfma_f32_32x32x16_f16 v[96:111], a[208:211], a[176:179], v[96:111]
	ds_read_b64_tr_b16 v[58:59], v225 offset:0x2c00
	v_cvt_pk_f16_f32 v53, v50, v51
	v_add_f32_e32 v32, v32, v50
	v_add_f32_e32 v33, v33, v51
	s_mov_b32 s34, s41
	v_mfma_f32_32x32x16_f16 v[80:95], a[240:243], a[144:147], v[80:95]
	ds_read_b64_tr_b16 v[48:49], v225 offset:0x2600
	v_cvt_pk_f16_f32 v54, v238, v239
	v_add_f32_e32 v32, v32, v238
	v_add_f32_e32 v33, v33, v239
	s_add_i32 s35, s31, 0x10400
	v_mfma_f32_32x32x16_f16 v[64:79], a[240:243], a[176:179], v[64:79]
	ds_read_b64_tr_b16 v[50:51], v225 offset:0x2e00
	ds_read_b64_tr_b16 v[44:45], v225 offset:0x3000
	v_cvt_pk_f16_f32 v55, v244, v245
	v_add_f32_e32 v32, v32, v244
	v_add_f32_e32 v33, v33, v245
	s_mov_b32 s91, s43
	v_mfma_f32_32x32x16_f16 v[112:127], a[212:215], a[148:151], v[112:127]
	ds_read_b64_tr_b16 v[46:47], v225 offset:0x3800
	v_add_f32_e32 v32, v32, v198
	v_add_f32_e32 v33, v33, v199
	s_add_i32 s30, s31, 0x10800
	s_mov_b32 s92, s30
	v_mfma_f32_32x32x16_f16 v[96:111], a[212:215], a[180:183], v[96:111]
	ds_read_b64_tr_b16 v[40:41], v225 offset:0x3200
	v_add_f32_e32 v32, v32, v232
	v_add_f32_e32 v33, v33, v233
	s_mov_b32 s93, s45
	v_mfma_f32_32x32x16_f16 v[80:95], a[244:247], a[148:151], v[80:95]
	ds_read_b64_tr_b16 v[42:43], v225 offset:0x3a00
	v_add_f32_e32 v32, v32, v234
	v_add_f32_e32 v33, v33, v235
	s_add_i32 s94, s31, 0x10c00
	v_mfma_f32_32x32x16_f16 v[64:79], a[244:247], a[180:183], v[64:79]
	ds_read_b64_tr_b16 v[36:37], v225 offset:0x3400
	ds_read_b64_tr_b16 v[38:39], v225 offset:0x3c00
	v_add_f32_e32 v156, v32, v236
	v_add_f32_e32 v157, v33, v237
	s_mov_b32 s95, s47
	v_mfma_f32_32x32x16_f16 v[112:127], a[216:219], a[152:155], v[112:127]
	ds_read_b64_tr_b16 v[32:33], v225 offset:0x3600
	v_cvt_pk_f16_f32 v140, v141, v142
	v_add_f32_e32 v158, v242, v141
	v_add_f32_e32 v142, v243, v142
	s_add_i32 s96, s31, 0xc000
	v_mfma_f32_32x32x16_f16 v[96:111], a[216:219], a[184:187], v[96:111]
	ds_read_b64_tr_b16 v[34:35], v225 offset:0x3e00
	v_cvt_pk_f16_f32 v141, v143, v246
	v_add_f32_e32 v143, v158, v143
	v_add_f32_e32 v158, v142, v246
	v_mfma_f32_32x32x16_f16 v[80:95], a[248:251], a[152:155], v[80:95]
	s_mov_b32 s97, s49
	v_cvt_pk_f16_f32 v142, v247, v248
	v_add_f32_e32 v159, v143, v247
	v_add_f32_e32 v158, v158, v248
	v_mfma_f32_32x32x16_f16 v[64:79], a[248:251], a[184:187], v[64:79]
	s_add_i32 s98, s31, 0xc080
	v_cvt_pk_f16_f32 v143, v249, v250
	v_add_f32_e32 v159, v159, v249
	v_add_f32_e32 v158, v158, v250
	v_mfma_f32_32x32x16_f16 v[112:127], a[220:223], a[156:159], v[112:127]
	s_mov_b32 s99, s51
	v_add_f32_e32 v159, v159, v148
	v_add_f32_e32 v158, v158, v149
	v_mfma_f32_32x32x16_f16 v[96:111], a[220:223], a[188:191], v[96:111]
	s_add_i32 vcc_lo, s31, 0xc800
	v_add_f32_e32 v159, v159, v150
	v_add_f32_e32 v158, v158, v151
	v_mfma_f32_32x32x16_f16 v[80:95], a[252:255], a[156:159], v[80:95]
	s_mov_b32 vcc_hi, s53
	v_add_f32_e32 v159, v159, v152
	v_add_f32_e32 v158, v158, v153
	v_mfma_f32_32x32x16_f16 v[64:79], a[252:255], a[188:191], v[64:79]
	s_add_i32 s80, s31, 0xc880
	v_add_f32_e32 v159, v159, v154
	v_add_f32_e32 v158, v158, v155
	s_nop 4
	v_add_f32_e32 v156, v156, v157
	s_waitcnt vmcnt(0) lgkmcnt(0)
	s_barrier
	v_mov_b32_e32 v157, v156
	s_nop 1
	v_permlane32_swap_b32_e32 v156, v157
	v_add_f32_e32 v156, v156, v157
	v_add_f32_e32 v197, v197, v156
	v_add_f32_e32 v156, v159, v158
	v_mov_b32_e32 v157, v156
	s_nop 1
	v_permlane32_swap_b32_e32 v156, v157
	v_add_f32_e32 v156, v156, v157
	v_add_f32_e32 v196, v196, v156
	s_nop 1
	v_mfma_f32_32x32x16_f16 a[0:15], v[180:183], v[164:167], a[0:15]
	s_mov_b32 m0, s0
	s_nop 0
	buffer_load_dwordx4 v211, s[16:19], s1 offen lds
	v_mfma_f32_32x32x16_f16 a[16:31], v[180:183], v[192:195], a[16:31]
	s_mov_b32 m0, s34
	s_nop 0
	buffer_load_dwordx4 v212, s[16:19], s35 offen lds
	ds_read_b128 a[192:195], v221 offset:0
	v_mfma_f32_32x32x16_f16 a[32:47], v[184:187], v[164:167], a[32:47]
	s_mov_b32 m0, s91
	s_nop 0
	buffer_load_dwordx4 v211, s[16:19], s92 offen lds
	ds_read_b128 a[196:199], v222 offset:0
	v_mfma_f32_32x32x16_f16 a[48:63], v[184:187], v[192:195], a[48:63]
	s_mov_b32 m0, s93
	s_nop 0
	buffer_load_dwordx4 v212, s[16:19], s94 offen lds
	ds_read_b128 a[200:203], v223 offset:0
	v_mfma_f32_32x32x16_f16 a[64:79], v[176:179], v[164:167], a[64:79]
	s_mov_b32 m0, s95
	s_nop 0
	buffer_load_dwordx4 v213, s[20:23], s96 offen lds
	ds_read_b128 a[204:207], v224 offset:0
	v_mfma_f32_32x32x16_f16 a[80:95], v[176:179], v[192:195], a[80:95]
	s_mov_b32 m0, s97
	s_nop 0
	buffer_load_dwordx4 v213, s[20:23], s98 offen lds
	ds_read_b128 a[208:211], v221 offset:128
	v_mfma_f32_32x32x16_f16 a[96:111], v[188:191], v[164:167], a[96:111]
	s_mov_b32 m0, s99
	s_nop 0
	buffer_load_dwordx4 v213, s[20:23], vcc_lo offen lds
	ds_read_b128 a[212:215], v222 offset:128
	v_mfma_f32_32x32x16_f16 a[112:127], v[188:191], v[192:195], a[112:127]
	s_mov_b32 m0, vcc_hi
	s_nop 0
	buffer_load_dwordx4 v213, s[20:23], s80 offen lds
	ds_read_b128 a[216:219], v223 offset:128
	v_mfma_f32_32x32x16_f16 a[0:15], v[172:175], v[128:131], a[0:15]
	ds_read_b128 a[220:223], v224 offset:128
	v_max3_f32 v156, v112, v113, v80
	v_max3_f32 v157, v114, v115, v81
	v_max3_f32 v156, v156, v82, v83
	v_mfma_f32_32x32x16_f16 a[16:31], v[172:175], v[144:147], a[16:31]
	ds_read_b128 a[224:227], v221 offset:8192
	v_max3_f32 v156, v156, v116, v117
	v_max3_f32 v157, v157, v118, v119
	v_max3_f32 v156, v156, v84, v85
	v_max3_f32 v157, v157, v86, v87
	v_mfma_f32_32x32x16_f16 a[32:47], v[168:171], v[128:131], a[32:47]
	ds_read_b128 a[228:231], v222 offset:8192
	v_max3_f32 v156, v156, v120, v121
	v_max3_f32 v157, v157, v122, v123
	v_max3_f32 v156, v156, v88, v89
	v_max3_f32 v157, v157, v90, v91
	v_mfma_f32_32x32x16_f16 a[48:63], v[168:171], v[144:147], a[48:63]
	ds_read_b128 a[232:235], v223 offset:8192
	v_max3_f32 v156, v156, v124, v125
	v_max3_f32 v157, v157, v126, v127
	v_max3_f32 v156, v156, v92, v93
	v_max3_f32 v157, v157, v94, v95
	v_mfma_f32_32x32x16_f16 a[64:79], v[160:163], v[128:131], a[64:79]
	ds_read_b128 a[236:239], v224 offset:8192
	v_max3_f32 v158, v96, v97, v64
	v_max3_f32 v159, v98, v99, v65
	v_max3_f32 v158, v158, v66, v67
	v_mfma_f32_32x32x16_f16 a[80:95], v[160:163], v[144:147], a[80:95]
	ds_read_b128 a[240:243], v221 offset:8320
	v_max3_f32 v158, v158, v100, v101
	v_max3_f32 v159, v159, v102, v103
	v_max3_f32 v158, v158, v68, v69
	v_max3_f32 v159, v159, v70, v71
	v_mfma_f32_32x32x16_f16 a[96:111], v[136:139], v[128:131], a[96:111]
	ds_read_b128 a[244:247], v222 offset:8320
	v_max3_f32 v128, v158, v104, v105
	v_max3_f32 v129, v159, v106, v107
	v_max3_f32 v128, v128, v72, v73
	v_max3_f32 v129, v129, v74, v75
	v_mfma_f32_32x32x16_f16 a[112:127], v[136:139], v[144:147], a[112:127]
	ds_read_b128 a[248:251], v223 offset:8320
	v_max3_f32 v128, v128, v108, v109
	v_max3_f32 v129, v129, v110, v111
	v_max3_f32 v128, v128, v76, v77
	v_max3_f32 v130, v129, v78, v79
	v_mfma_f32_32x32x16_f16 a[0:15], v[132:135], v[52:55], a[0:15]
	ds_read_b128 a[252:255], v224 offset:8320
	v_max_f32_e32 v129, v156, v157
	v_mov_b32_e32 v131, v129
	s_nop 1
	v_permlane32_swap_b32_e32 v129, v131
	v_max_f32_e32 v129, v129, v131
	v_mfma_f32_32x32x16_f16 a[16:31], v[132:135], v[140:143], a[16:31]
	v_max_f32_e32 v128, v128, v130
	v_mov_b32_e32 v130, v128
	s_nop 1
	v_permlane32_swap_b32_e32 v128, v130
	v_max_f32_e32 v128, v128, v130
	v_max_f32_e32 v130, v129, v128
	v_mfma_f32_32x32x16_f16 a[32:47], v[60:63], v[52:55], a[32:47]
	v_cmp_lt_f32_e32 vcc, s79, v130
	s_cmp_lg_u64 vcc, 0
	s_cselect_b64 s[0:1], -1, 0
	s_cbranch_vccnz .LBB3_17

.LBB3_14:
	s_waitcnt lgkmcnt(0)
	v_exp_f32_e32 v80, v80
	v_exp_f32_e32 v81, v81
	v_mfma_f32_32x32x16_f16 v[112:127], a[192:195], a[128:131], v[16:31]
	ds_read_b64_tr_b16 v[180:181], v210 offset:0
	v_cvt_pk_f16_f32 v164, v128, v129
	v_exp_f32_e32 v82, v82
	v_exp_f32_e32 v83, v83
	v_mfma_f32_32x32x16_f16 v[96:111], a[192:195], a[160:163], v[0:15]
	ds_read_b64_tr_b16 v[182:183], v210 offset:0x800
	v_cvt_pk_f16_f32 v165, v130, v131
	v_mfma_f32_32x32x16_f16 v[48:63], a[224:227], a[128:131], v[16:31]
	ds_read_b64_tr_b16 v[184:185], v210 offset:0x200
	v_exp_f32_e32 v242, v84
	v_exp_f32_e32 v243, v85
	v_cvt_pk_f16_f32 v166, v132, v133
	v_mfma_f32_32x32x16_f16 v[32:47], a[224:227], a[160:163], v[0:15]
	ds_read_b64_tr_b16 v[186:187], v210 offset:0xa00
	ds_read_b64_tr_b16 v[176:177], v210 offset:0x400
	v_exp_f32_e32 v244, v86
	v_exp_f32_e32 v245, v87
	v_cvt_pk_f16_f32 v167, v134, v135
	v_exp_f32_e32 v198, v88
	v_exp_f32_e32 v199, v89
	v_mfma_f32_32x32x16_f16 v[112:127], a[196:199], a[132:135], v[112:127]
	ds_read_b64_tr_b16 v[178:179], v210 offset:0xc00
	v_cvt_pk_f16_f32 v128, v136, v137
	v_exp_f32_e32 v232, v90
	v_exp_f32_e32 v233, v91
	v_mfma_f32_32x32x16_f16 v[96:111], a[196:199], a[164:167], v[96:111]
	ds_read_b64_tr_b16 v[188:189], v210 offset:0x600
	v_cvt_pk_f16_f32 v129, v138, v139
	v_exp_f32_e32 v234, v92
	v_exp_f32_e32 v235, v93
	v_mfma_f32_32x32x16_f16 v[48:63], a[228:231], a[132:135], v[48:63]
	ds_read_b64_tr_b16 v[190:191], v210 offset:0xe00
	v_cvt_pk_f16_f32 v130, v140, v141
	v_mfma_f32_32x32x16_f16 v[32:47], a[228:231], a[164:167], v[32:47]
	ds_read_b64_tr_b16 v[172:173], v210 offset:0x1000
	v_exp_f32_e32 v236, v94
	v_exp_f32_e32 v237, v95
	ds_read_b64_tr_b16 v[174:175], v210 offset:0x1800
	v_cvt_pk_f16_f32 v131, v142, v143
	v_exp_f32_e32 v141, v64
	v_exp_f32_e32 v142, v65
	v_mfma_f32_32x32x16_f16 v[112:127], a[200:203], a[136:139], v[112:127]
	ds_read_b64_tr_b16 v[168:169], v210 offset:0x1200
	v_cvt_pk_f16_f32 v192, v144, v145
	v_exp_f32_e32 v143, v66
	v_mfma_f32_32x32x16_f16 v[96:111], a[200:203], a[168:171], v[96:111]
	ds_read_b64_tr_b16 v[170:171], v210 offset:0x1a00
	v_exp_f32_e32 v246, v67
	v_cvt_pk_f16_f32 v193, v146, v147
	v_mfma_f32_32x32x16_f16 v[48:63], a[232:235], a[136:139], v[48:63]
	ds_read_b64_tr_b16 v[160:161], v210 offset:0x1400
	v_exp_f32_e32 v247, v68
	v_exp_f32_e32 v248, v69
	v_cvt_pk_f16_f32 v194, v148, v149
	v_mfma_f32_32x32x16_f16 v[32:47], a[232:235], a[168:171], v[32:47]
	ds_read_b64_tr_b16 v[162:163], v210 offset:0x1c00
	ds_read_b64_tr_b16 v[136:137], v210 offset:0x1600
	v_exp_f32_e32 v249, v70
	v_exp_f32_e32 v250, v71
	v_cvt_pk_f16_f32 v195, v150, v151
	v_exp_f32_e32 v148, v72
	v_exp_f32_e32 v149, v73
	v_mfma_f32_32x32x16_f16 v[112:127], a[204:207], a[140:143], v[112:127]
	ds_read_b64_tr_b16 v[138:139], v210 offset:0x1e00
	v_cvt_pk_f16_f32 v144, v152, v153
	v_exp_f32_e32 v150, v74
	v_exp_f32_e32 v151, v75
	v_mfma_f32_32x32x16_f16 v[96:111], a[204:207], a[172:175], v[96:111]
	ds_read_b64_tr_b16 v[132:133], v210 offset:0x2000
	v_cvt_pk_f16_f32 v145, v154, v155
	v_exp_f32_e32 v152, v76
	v_exp_f32_e32 v153, v77
	v_mfma_f32_32x32x16_f16 v[48:63], a[236:239], a[140:143], v[48:63]
	ds_read_b64_tr_b16 v[134:135], v210 offset:0x2800
	v_cvt_pk_f16_f32 v146, v156, v157
	v_mfma_f32_32x32x16_f16 v[32:47], a[236:239], a[172:175], v[32:47]
	ds_read_b64_tr_b16 v[92:93], v210 offset:0x2200
	v_exp_f32_e32 v154, v78
	v_exp_f32_e32 v155, v79
	ds_read_b64_tr_b16 v[94:95], v210 offset:0x2a00
	v_cvt_pk_f16_f32 v147, v158, v159
	s_mov_b32 s0, s55
	v_mfma_f32_32x32x16_f16 v[112:127], a[208:211], a[144:147], v[112:127]
	ds_read_b64_tr_b16 v[88:89], v210 offset:0x2400
	v_cvt_pk_f16_f32 v84, v80, v81
	v_add_f32_e32 v64, v239, v80
	v_add_f32_e32 v65, v238, v81
	s_add_i32 s1, s31, 0x14000
	v_mfma_f32_32x32x16_f16 v[96:111], a[208:211], a[176:179], v[96:111]
	ds_read_b64_tr_b16 v[90:91], v210 offset:0x2c00
	v_cvt_pk_f16_f32 v85, v82, v83
	v_add_f32_e32 v64, v64, v82
	v_add_f32_e32 v65, v65, v83
	s_mov_b32 s34, s57
	v_mfma_f32_32x32x16_f16 v[48:63], a[240:243], a[144:147], v[48:63]
	ds_read_b64_tr_b16 v[80:81], v210 offset:0x2600
	v_cvt_pk_f16_f32 v86, v242, v243
	v_add_f32_e32 v64, v64, v242
	v_add_f32_e32 v65, v65, v243
	s_add_i32 s35, s31, 0x14400
	v_mfma_f32_32x32x16_f16 v[32:47], a[240:243], a[176:179], v[32:47]
	ds_read_b64_tr_b16 v[82:83], v210 offset:0x2e00
	ds_read_b64_tr_b16 v[76:77], v210 offset:0x3000
	v_cvt_pk_f16_f32 v87, v244, v245
	v_add_f32_e32 v64, v64, v244
	v_add_f32_e32 v65, v65, v245
	s_mov_b32 s91, s59
	v_mfma_f32_32x32x16_f16 v[112:127], a[212:215], a[148:151], v[112:127]
	ds_read_b64_tr_b16 v[78:79], v210 offset:0x3800
	v_add_f32_e32 v64, v64, v198
	v_add_f32_e32 v65, v65, v199
	s_add_i32 s92, s31, 0x14800
	v_mfma_f32_32x32x16_f16 v[96:111], a[212:215], a[180:183], v[96:111]
	ds_read_b64_tr_b16 v[72:73], v210 offset:0x3200
	v_add_f32_e32 v64, v64, v232
	v_add_f32_e32 v65, v65, v233
	s_mov_b32 s93, s61
	v_mfma_f32_32x32x16_f16 v[48:63], a[244:247], a[148:151], v[48:63]
	ds_read_b64_tr_b16 v[74:75], v210 offset:0x3a00
	v_add_f32_e32 v64, v64, v234
	v_add_f32_e32 v65, v65, v235
	s_add_i32 s94, s31, 0x14c00
	v_mfma_f32_32x32x16_f16 v[32:47], a[244:247], a[180:183], v[32:47]
	ds_read_b64_tr_b16 v[68:69], v210 offset:0x3400
	ds_read_b64_tr_b16 v[70:71], v210 offset:0x3c00
	v_add_f32_e32 v156, v64, v236
	v_add_f32_e32 v157, v65, v237
	s_mov_b32 s95, s38
	v_mfma_f32_32x32x16_f16 v[112:127], a[216:219], a[152:155], v[112:127]
	ds_read_b64_tr_b16 v[64:65], v210 offset:0x3600
	v_cvt_pk_f16_f32 v140, v141, v142
	v_add_f32_e32 v158, v240, v141
	v_add_f32_e32 v142, v241, v142
	v_mfma_f32_32x32x16_f16 v[96:111], a[216:219], a[184:187], v[96:111]
	ds_read_b64_tr_b16 v[66:67], v210 offset:0x3e00
	v_cvt_pk_f16_f32 v141, v143, v246
	v_add_f32_e32 v143, v158, v143
	v_add_f32_e32 v158, v142, v246
	v_mfma_f32_32x32x16_f16 v[48:63], a[248:251], a[152:155], v[48:63]
	s_mov_b32 s80, s63
	v_cvt_pk_f16_f32 v142, v247, v248
	v_add_f32_e32 v159, v143, v247
	v_add_f32_e32 v158, v158, v248
	v_mfma_f32_32x32x16_f16 v[32:47], a[248:251], a[184:187], v[32:47]
	s_add_i32 s96, s31, 0x10080
	v_cvt_pk_f16_f32 v143, v249, v250
	v_add_f32_e32 v159, v159, v249
	v_add_f32_e32 v158, v158, v250
	v_mfma_f32_32x32x16_f16 v[112:127], a[220:223], a[156:159], v[112:127]
	s_mov_b32 s97, s65
	v_add_f32_e32 v159, v159, v148
	v_add_f32_e32 v158, v158, v149
	v_mfma_f32_32x32x16_f16 v[96:111], a[220:223], a[188:191], v[96:111]
	v_add_f32_e32 v159, v159, v150
	v_add_f32_e32 v158, v158, v151
	v_mfma_f32_32x32x16_f16 v[48:63], a[252:255], a[156:159], v[48:63]
	s_mov_b32 s98, s66
	v_add_f32_e32 v159, v159, v152
	v_add_f32_e32 v158, v158, v153
	v_mfma_f32_32x32x16_f16 v[32:47], a[252:255], a[188:191], v[32:47]
	s_add_i32 s31, s31, 0x10880
	v_add_f32_e32 v159, v159, v154
	v_add_f32_e32 v158, v158, v155
	s_nop 4
	v_add_f32_e32 v156, v156, v157
	s_waitcnt vmcnt(0) lgkmcnt(0)
	s_barrier
	v_mov_b32_e32 v157, v156
	s_nop 1
	v_permlane32_swap_b32_e32 v156, v157
	v_add_f32_e32 v156, v156, v157
	v_add_f32_e32 v197, v197, v156
	v_add_f32_e32 v156, v159, v158
	v_mov_b32_e32 v157, v156
	s_nop 1
	v_permlane32_swap_b32_e32 v156, v157
	v_add_f32_e32 v156, v156, v157
	v_add_f32_e32 v196, v196, v156
	s_nop 1
	v_mfma_f32_32x32x16_f16 a[0:15], v[180:183], v[164:167], a[0:15]
	s_mov_b32 m0, s0
	s_nop 0
	buffer_load_dwordx4 v211, s[16:19], s1 offen lds
	v_mfma_f32_32x32x16_f16 a[16:31], v[180:183], v[192:195], a[16:31]
	s_mov_b32 m0, s34
	s_nop 0
	buffer_load_dwordx4 v212, s[16:19], s35 offen lds
	ds_read_b128 a[192:195], v206 offset:0
	v_mfma_f32_32x32x16_f16 a[32:47], v[184:187], v[164:167], a[32:47]
	s_mov_b32 m0, s91
	s_nop 0
	buffer_load_dwordx4 v211, s[16:19], s92 offen lds
	ds_read_b128 a[196:199], v207 offset:0
	v_mfma_f32_32x32x16_f16 a[48:63], v[184:187], v[192:195], a[48:63]
	s_mov_b32 m0, s93
	s_nop 0
	buffer_load_dwordx4 v212, s[16:19], s94 offen lds
	ds_read_b128 a[200:203], v208 offset:0
	v_mfma_f32_32x32x16_f16 a[64:79], v[176:179], v[164:167], a[64:79]
	s_mov_b32 m0, s95
	s_nop 0
	buffer_load_dwordx4 v213, s[20:23], s24 offen lds
	ds_read_b128 a[204:207], v209 offset:0
	v_mfma_f32_32x32x16_f16 a[80:95], v[176:179], v[192:195], a[80:95]
	s_mov_b32 m0, s80
	s_nop 0
	buffer_load_dwordx4 v213, s[20:23], s96 offen lds
	ds_read_b128 a[208:211], v206 offset:128
	v_mfma_f32_32x32x16_f16 a[96:111], v[188:191], v[164:167], a[96:111]
	s_mov_b32 m0, s97
	s_nop 0
	buffer_load_dwordx4 v213, s[20:23], s30 offen lds
	ds_read_b128 a[212:215], v207 offset:128
	v_mfma_f32_32x32x16_f16 a[112:127], v[188:191], v[192:195], a[112:127]
	s_mov_b32 m0, s98
	s_nop 0
	buffer_load_dwordx4 v213, s[20:23], s31 offen lds
	ds_read_b128 a[216:219], v208 offset:128
	v_mfma_f32_32x32x16_f16 a[0:15], v[172:175], v[128:131], a[0:15]
	ds_read_b128 a[220:223], v209 offset:128
	v_max3_f32 v156, v112, v113, v48
	v_max3_f32 v157, v114, v115, v49
	v_max3_f32 v156, v156, v50, v51
	v_mfma_f32_32x32x16_f16 a[16:31], v[172:175], v[144:147], a[16:31]
	ds_read_b128 a[224:227], v206 offset:8192
	v_max3_f32 v156, v156, v116, v117
	v_max3_f32 v157, v157, v118, v119
	v_max3_f32 v156, v156, v52, v53
	v_max3_f32 v157, v157, v54, v55
	v_mfma_f32_32x32x16_f16 a[32:47], v[168:171], v[128:131], a[32:47]
	ds_read_b128 a[228:231], v207 offset:8192
	v_max3_f32 v156, v156, v120, v121
	v_max3_f32 v157, v157, v122, v123
	v_max3_f32 v156, v156, v56, v57
	v_max3_f32 v157, v157, v58, v59
	v_mfma_f32_32x32x16_f16 a[48:63], v[168:171], v[144:147], a[48:63]
	ds_read_b128 a[232:235], v208 offset:8192
	v_max3_f32 v156, v156, v124, v125
	v_max3_f32 v157, v157, v126, v127
	v_max3_f32 v156, v156, v60, v61
	v_max3_f32 v157, v157, v62, v63
	v_mfma_f32_32x32x16_f16 a[64:79], v[160:163], v[128:131], a[64:79]
	ds_read_b128 a[236:239], v209 offset:8192
	v_max3_f32 v158, v96, v97, v32
	v_max3_f32 v159, v98, v99, v33
	v_max3_f32 v158, v158, v34, v35
	v_mfma_f32_32x32x16_f16 a[80:95], v[160:163], v[144:147], a[80:95]
	ds_read_b128 a[240:243], v206 offset:8320
	v_max3_f32 v158, v158, v100, v101
	v_max3_f32 v159, v159, v102, v103
	v_max3_f32 v158, v158, v36, v37
	v_max3_f32 v159, v159, v38, v39
	v_mfma_f32_32x32x16_f16 a[96:111], v[136:139], v[128:131], a[96:111]
	ds_read_b128 a[244:247], v207 offset:8320
	v_max3_f32 v128, v158, v104, v105
	v_max3_f32 v129, v159, v106, v107
	v_max3_f32 v128, v128, v40, v41
	v_max3_f32 v129, v129, v42, v43
	v_mfma_f32_32x32x16_f16 a[112:127], v[136:139], v[144:147], a[112:127]
	ds_read_b128 a[248:251], v208 offset:8320
	v_max3_f32 v128, v128, v108, v109
	v_max3_f32 v129, v129, v110, v111
	v_max3_f32 v128, v128, v44, v45
	v_max3_f32 v130, v129, v46, v47
	v_mfma_f32_32x32x16_f16 a[0:15], v[132:135], v[84:87], a[0:15]
	ds_read_b128 a[252:255], v209 offset:8320
	v_max_f32_e32 v129, v156, v157
	v_mov_b32_e32 v131, v129
	s_nop 1
	v_permlane32_swap_b32_e32 v129, v131
	v_max_f32_e32 v129, v129, v131
	v_mfma_f32_32x32x16_f16 a[16:31], v[132:135], v[140:143], a[16:31]
	v_max_f32_e32 v128, v128, v130
	v_mov_b32_e32 v130, v128
	s_nop 1
	v_permlane32_swap_b32_e32 v128, v130
	v_max_f32_e32 v128, v128, v130
	v_max_f32_e32 v130, v129, v128
	v_mfma_f32_32x32x16_f16 a[32:47], v[92:95], v[84:87], a[32:47]
	v_cmp_lt_f32_e32 vcc, s79, v130
	s_cmp_lg_u64 vcc, 0
	s_cselect_b64 s[0:1], -1, 0
	s_cbranch_vccnz .LBB3_19

.LBB3_21:
	s_add_u32 s30, s28, s39
	s_addc_u32 s31, s29, 0
	v_cmp_lt_u64_e32 vcc, s[30:31], v[202:203]
	s_and_b64 s[0:1], vcc, exec
	s_cselect_b32 s0, s30, s28
	s_and_b32 s1, s0, 15
	s_lshl_b32 s12, s0, 4
	s_lshr_b32 s0, s0, 3
	s_and_b32 s0, s0, 0x1ffffff0
	s_or_b32 s24, s1, s0
	s_and_b32 s12, s12, 0x700
	s_lshl_b64 s[34:35], s[24:25], 19
	v_exp_f32_e32 v48, v48
	v_exp_f32_e32 v49, v49
	s_add_u32 s16, s6, s34
	v_mfma_f32_32x32x16_f16 v[112:127], a[192:195], a[128:131], v[16:31]
	ds_read_b64_tr_b16 v[180:181], v225 offset:0
	v_or_b32_e32 v64, s12, v215
	s_addc_u32 s0, s7, s35
	s_and_b32 s17, s0, 0xffff
	v_readfirstlane_b32 s24, v64
	s_mov_b32 s12, s16
	s_mov_b32 s13, s17
	v_cvt_pk_f16_f32 v164, v128, v129
	v_exp_f32_e32 v50, v50
	v_exp_f32_e32 v51, v51
	v_mfma_f32_32x32x16_f16 v[96:111], a[192:195], a[160:163], v[0:15]
	ds_read_b64_tr_b16 v[182:183], v225 offset:0x800
	v_cvt_pk_f16_f32 v165, v130, v131
	v_exp_f32_e32 v232, v52
	v_exp_f32_e32 v233, v53
	v_mfma_f32_32x32x16_f16 v[80:95], a[224:227], a[128:131], v[16:31]
	ds_read_b64_tr_b16 v[184:185], v225 offset:0x200
	v_cvt_pk_f16_f32 v166, v132, v133
	v_mfma_f32_32x32x16_f16 v[64:79], a[224:227], a[160:163], v[0:15]
	ds_read_b64_tr_b16 v[186:187], v225 offset:0xa00
	ds_read_b64_tr_b16 v[176:177], v225 offset:0x400
	v_exp_f32_e32 v244, v54
	v_exp_f32_e32 v245, v55
	v_cvt_pk_f16_f32 v167, v134, v135
	v_exp_f32_e32 v198, v56
	v_exp_f32_e32 v199, v57
	v_mfma_f32_32x32x16_f16 v[112:127], a[196:199], a[132:135], v[112:127]
	ds_read_b64_tr_b16 v[178:179], v225 offset:0xc00
	v_cvt_pk_f16_f32 v128, v136, v137
	v_exp_f32_e32 v234, v58
	v_exp_f32_e32 v235, v59
	v_mfma_f32_32x32x16_f16 v[96:111], a[196:199], a[164:167], v[96:111]
	ds_read_b64_tr_b16 v[188:189], v225 offset:0x600
	v_cvt_pk_f16_f32 v129, v138, v139
	v_exp_f32_e32 v236, v60
	v_exp_f32_e32 v237, v61
	v_mfma_f32_32x32x16_f16 v[80:95], a[228:231], a[132:135], v[80:95]
	ds_read_b64_tr_b16 v[190:191], v225 offset:0xe00
	v_cvt_pk_f16_f32 v130, v140, v141
	v_mfma_f32_32x32x16_f16 v[64:79], a[228:231], a[164:167], v[64:79]
	ds_read_b64_tr_b16 v[172:173], v225 offset:0x1000
	v_exp_f32_e32 v238, v62
	v_exp_f32_e32 v239, v63
	ds_read_b64_tr_b16 v[174:175], v225 offset:0x1800
	v_cvt_pk_f16_f32 v131, v142, v143
	v_exp_f32_e32 v141, v32
	v_exp_f32_e32 v142, v33
	v_mfma_f32_32x32x16_f16 v[112:127], a[200:203], a[136:139], v[112:127]
	ds_read_b64_tr_b16 v[168:169], v225 offset:0x1200
	v_cvt_pk_f16_f32 v192, v144, v145
	v_exp_f32_e32 v143, v34
	v_mfma_f32_32x32x16_f16 v[96:111], a[200:203], a[168:171], v[96:111]
	ds_read_b64_tr_b16 v[170:171], v225 offset:0x1a00
	v_exp_f32_e32 v246, v35
	v_cvt_pk_f16_f32 v193, v146, v147
	v_mfma_f32_32x32x16_f16 v[80:95], a[232:235], a[136:139], v[80:95]
	ds_read_b64_tr_b16 v[160:161], v225 offset:0x1400
	v_exp_f32_e32 v247, v36
	v_exp_f32_e32 v248, v37
	v_cvt_pk_f16_f32 v194, v148, v149
	v_mfma_f32_32x32x16_f16 v[64:79], a[232:235], a[168:171], v[64:79]
	ds_read_b64_tr_b16 v[162:163], v225 offset:0x1c00
	ds_read_b64_tr_b16 v[136:137], v225 offset:0x1600
	v_exp_f32_e32 v249, v38
	v_exp_f32_e32 v250, v39
	v_cvt_pk_f16_f32 v195, v150, v151
	v_exp_f32_e32 v148, v40
	v_exp_f32_e32 v149, v41
	v_mfma_f32_32x32x16_f16 v[112:127], a[204:207], a[140:143], v[112:127]
	ds_read_b64_tr_b16 v[138:139], v225 offset:0x1e00
	v_cvt_pk_f16_f32 v144, v152, v153
	v_exp_f32_e32 v150, v42
	v_exp_f32_e32 v151, v43
	v_mfma_f32_32x32x16_f16 v[96:111], a[204:207], a[172:175], v[96:111]
	ds_read_b64_tr_b16 v[132:133], v225 offset:0x2000
	v_cvt_pk_f16_f32 v145, v154, v155
	v_exp_f32_e32 v152, v44
	v_exp_f32_e32 v153, v45
	v_mfma_f32_32x32x16_f16 v[80:95], a[236:239], a[140:143], v[80:95]
	ds_read_b64_tr_b16 v[134:135], v225 offset:0x2800
	v_cvt_pk_f16_f32 v146, v156, v157
	v_mfma_f32_32x32x16_f16 v[64:79], a[236:239], a[172:175], v[64:79]
	ds_read_b64_tr_b16 v[60:61], v225 offset:0x2200
	v_exp_f32_e32 v154, v46
	v_exp_f32_e32 v155, v47
	ds_read_b64_tr_b16 v[62:63], v225 offset:0x2a00
	v_cvt_pk_f16_f32 v147, v158, v159
	s_mov_b32 s0, s33
	v_mfma_f32_32x32x16_f16 v[112:127], a[208:211], a[144:147], v[112:127]
	ds_read_b64_tr_b16 v[56:57], v225 offset:0x2400
	v_cvt_pk_f16_f32 v52, v48, v49
	v_add_f32_e32 v32, v241, v48
	v_add_f32_e32 v33, v240, v49
	s_mov_b32 s1, s36
	v_mfma_f32_32x32x16_f16 v[96:111], a[208:211], a[176:179], v[96:111]
	ds_read_b64_tr_b16 v[58:59], v225 offset:0x2c00
	v_cvt_pk_f16_f32 v53, v50, v51
	v_add_f32_e32 v32, v32, v50
	v_add_f32_e32 v33, v33, v51
	s_mov_b32 s22, s41
	v_mfma_f32_32x32x16_f16 v[80:95], a[240:243], a[144:147], v[80:95]
	ds_read_b64_tr_b16 v[48:49], v225 offset:0x2600
	v_cvt_pk_f16_f32 v54, v232, v233
	v_add_f32_e32 v32, v32, v232
	v_add_f32_e32 v33, v33, v233
	s_mov_b32 s23, s68
	v_mfma_f32_32x32x16_f16 v[64:79], a[240:243], a[176:179], v[64:79]
	ds_read_b64_tr_b16 v[50:51], v225 offset:0x2e00
	ds_read_b64_tr_b16 v[44:45], v225 offset:0x3000
	v_cvt_pk_f16_f32 v55, v244, v245
	v_add_f32_e32 v32, v32, v244
	v_add_f32_e32 v33, v33, v245
	s_mov_b32 s29, s43
	v_mfma_f32_32x32x16_f16 v[112:127], a[212:215], a[148:151], v[112:127]
	ds_read_b64_tr_b16 v[46:47], v225 offset:0x3800
	v_add_f32_e32 v32, v32, v198
	v_add_f32_e32 v33, v33, v199
	s_mov_b32 s91, s69
	v_mfma_f32_32x32x16_f16 v[96:111], a[212:215], a[180:183], v[96:111]
	ds_read_b64_tr_b16 v[40:41], v225 offset:0x3200
	v_add_f32_e32 v32, v32, v234
	v_add_f32_e32 v33, v33, v235
	s_mov_b32 s92, s45
	v_mfma_f32_32x32x16_f16 v[80:95], a[244:247], a[148:151], v[80:95]
	ds_read_b64_tr_b16 v[42:43], v225 offset:0x3a00
	v_add_f32_e32 v32, v32, v236
	v_add_f32_e32 v33, v33, v237
	s_mov_b32 s94, s70
	v_mfma_f32_32x32x16_f16 v[64:79], a[244:247], a[180:183], v[64:79]
	ds_read_b64_tr_b16 v[36:37], v225 offset:0x3400
	ds_read_b64_tr_b16 v[38:39], v225 offset:0x3c00
	v_add_f32_e32 v156, v32, v238
	v_add_f32_e32 v157, v33, v239
	s_mov_b32 s93, s47
	v_mfma_f32_32x32x16_f16 v[112:127], a[216:219], a[152:155], v[112:127]
	ds_read_b64_tr_b16 v[32:33], v225 offset:0x3600
	v_cvt_pk_f16_f32 v140, v141, v142
	v_add_f32_e32 v158, v242, v141
	v_add_f32_e32 v142, v243, v142
	s_mov_b32 s95, s71
	v_mfma_f32_32x32x16_f16 v[96:111], a[216:219], a[184:187], v[96:111]
	ds_read_b64_tr_b16 v[34:35], v225 offset:0x3e00
	v_cvt_pk_f16_f32 v141, v143, v246
	v_add_f32_e32 v143, v158, v143
	v_add_f32_e32 v158, v142, v246
	v_mfma_f32_32x32x16_f16 v[80:95], a[248:251], a[152:155], v[80:95]
	s_mov_b32 s96, s49
	v_cvt_pk_f16_f32 v142, v247, v248
	v_add_f32_e32 v159, v143, v247
	v_add_f32_e32 v158, v158, v248
	v_mfma_f32_32x32x16_f16 v[64:79], a[248:251], a[184:187], v[64:79]
	s_mov_b32 s97, s72
	v_cvt_pk_f16_f32 v143, v249, v250
	v_add_f32_e32 v159, v159, v249
	v_add_f32_e32 v158, v158, v250
	v_mfma_f32_32x32x16_f16 v[112:127], a[220:223], a[156:159], v[112:127]
	s_mov_b32 s98, s51
	v_add_f32_e32 v159, v159, v148
	v_add_f32_e32 v158, v158, v149
	v_mfma_f32_32x32x16_f16 v[96:111], a[220:223], a[188:191], v[96:111]
	s_mov_b32 s99, s73
	v_add_f32_e32 v159, v159, v150
	v_add_f32_e32 v158, v158, v151
	v_mfma_f32_32x32x16_f16 v[80:95], a[252:255], a[156:159], v[80:95]
	s_mov_b32 vcc_lo, s53
	v_add_f32_e32 v159, v159, v152
	v_add_f32_e32 v158, v158, v153
	v_mfma_f32_32x32x16_f16 v[64:79], a[252:255], a[188:191], v[64:79]
	s_mov_b32 vcc_hi, s74
	v_add_f32_e32 v159, v159, v154
	v_add_f32_e32 v158, v158, v155
	s_nop 0
	s_nop 4
	v_add_f32_e32 v156, v156, v157
	s_waitcnt vmcnt(0) lgkmcnt(0)
	s_barrier
	s_nop 0
	v_mov_b32_e32 v157, v156
	s_nop 1
	v_permlane32_swap_b32_e32 v156, v157
	v_add_f32_e32 v156, v156, v157
	s_nop 0
	v_add_f32_e32 v233, v197, v156
	v_add_f32_e32 v156, v159, v158
	s_nop 0
	v_mov_b32_e32 v157, v156
	s_nop 1
	v_permlane32_swap_b32_e32 v156, v157
	v_add_f32_e32 v156, v156, v157
	s_nop 0
	v_add_f32_e32 v232, v196, v156
	s_nop 1
	v_mfma_f32_32x32x16_f16 a[0:15], v[180:183], v[164:167], a[0:15]
	s_nop 0
	v_mfma_f32_32x32x16_f16 a[16:31], v[180:183], v[192:195], a[16:31]
	ds_read_b128 a[192:195], v221 offset:0
	s_nop 0
	v_mfma_f32_32x32x16_f16 a[32:47], v[184:187], v[164:167], a[32:47]
	ds_read_b128 a[196:199], v222 offset:0
	s_nop 0
	v_mfma_f32_32x32x16_f16 a[48:63], v[184:187], v[192:195], a[48:63]
	ds_read_b128 a[200:203], v223 offset:0
	s_nop 0
	v_mfma_f32_32x32x16_f16 a[64:79], v[176:179], v[164:167], a[64:79]
	s_mov_b32 s22, s18
	s_mov_b32 s23, s19
	s_mov_b32 m0, s93
	s_nop 0
	buffer_load_dwordx4 v213, s[20:23], s95 offen lds
	ds_read_b128 a[204:207], v224 offset:0
	v_mfma_f32_32x32x16_f16 a[80:95], v[176:179], v[192:195], a[80:95]
	s_nop 0
	s_mov_b32 m0, s96
	s_nop 0
	buffer_load_dwordx4 v213, s[20:23], s97 offen lds
	ds_read_b128 a[208:211], v221 offset:128
	v_mfma_f32_32x32x16_f16 a[96:111], v[188:191], v[164:167], a[96:111]
	s_nop 0
	s_mov_b32 m0, s98
	s_nop 0
	buffer_load_dwordx4 v213, s[20:23], s99 offen lds
	ds_read_b128 a[212:215], v222 offset:128
	v_mfma_f32_32x32x16_f16 a[112:127], v[188:191], v[192:195], a[112:127]
	s_nop 0
	s_mov_b32 m0, vcc_lo
	s_nop 0
	buffer_load_dwordx4 v213, s[20:23], vcc_hi offen lds
	ds_read_b128 a[216:219], v223 offset:128
	v_mfma_f32_32x32x16_f16 a[0:15], v[172:175], v[128:131], a[0:15]
	s_nop 0
	ds_read_b128 a[220:223], v224 offset:128
	v_max3_f32 v156, v112, v113, v80
	v_max3_f32 v157, v114, v115, v81
	s_nop 0
	v_max3_f32 v156, v156, v82, v83
	v_mfma_f32_32x32x16_f16 a[16:31], v[172:175], v[144:147], a[16:31]
	ds_read_b128 a[224:227], v221 offset:8192
	s_nop 0
	v_max3_f32 v156, v156, v116, v117
	v_max3_f32 v157, v157, v118, v119
	s_nop 0
	v_max3_f32 v156, v156, v84, v85
	v_max3_f32 v157, v157, v86, v87
	v_mfma_f32_32x32x16_f16 a[32:47], v[168:171], v[128:131], a[32:47]
	ds_read_b128 a[228:231], v222 offset:8192
	s_nop 0
	v_max3_f32 v156, v156, v120, v121
	v_max3_f32 v157, v157, v122, v123
	s_nop 0
	v_max3_f32 v156, v156, v88, v89
	v_max3_f32 v157, v157, v90, v91
	v_mfma_f32_32x32x16_f16 a[48:63], v[168:171], v[144:147], a[48:63]
	ds_read_b128 a[232:235], v223 offset:8192
	s_nop 0
	v_max3_f32 v156, v156, v124, v125
	v_max3_f32 v157, v157, v126, v127
	s_nop 0
	v_max3_f32 v156, v156, v92, v93
	v_max3_f32 v157, v157, v94, v95
	v_mfma_f32_32x32x16_f16 a[64:79], v[160:163], v[128:131], a[64:79]
	ds_read_b128 a[236:239], v224 offset:8192
	v_max3_f32 v158, v96, v97, v64
	v_max3_f32 v159, v98, v99, v65
	s_nop 0
	v_max3_f32 v158, v158, v66, v67
	v_mfma_f32_32x32x16_f16 a[80:95], v[160:163], v[144:147], a[80:95]
	ds_read_b128 a[240:243], v221 offset:8320
	s_nop 0
	v_max3_f32 v158, v158, v100, v101
	v_max3_f32 v159, v159, v102, v103
	s_nop 0
	v_max3_f32 v158, v158, v68, v69
	v_max3_f32 v159, v159, v70, v71
	v_mfma_f32_32x32x16_f16 a[96:111], v[136:139], v[128:131], a[96:111]
	ds_read_b128 a[244:247], v222 offset:8320
	s_nop 0
	v_max3_f32 v128, v158, v104, v105
	v_max3_f32 v129, v159, v106, v107
	s_nop 0
	v_max3_f32 v128, v128, v72, v73
	v_max3_f32 v129, v129, v74, v75
	v_mfma_f32_32x32x16_f16 a[112:127], v[136:139], v[144:147], a[112:127]
	ds_read_b128 a[248:251], v223 offset:8320
	s_nop 0
	v_max3_f32 v128, v128, v108, v109
	v_max3_f32 v129, v129, v110, v111
	s_nop 0
	v_max3_f32 v128, v128, v76, v77
	v_max3_f32 v130, v129, v78, v79
	v_mfma_f32_32x32x16_f16 a[0:15], v[132:135], v[52:55], a[0:15]
	ds_read_b128 a[252:255], v224 offset:8320
	v_max_f32_e32 v129, v156, v157
	s_nop 0
	v_mov_b32_e32 v131, v129
	s_nop 1
	v_permlane32_swap_b32_e32 v129, v131
	v_max_f32_e32 v129, v129, v131
	v_mfma_f32_32x32x16_f16 a[16:31], v[132:135], v[140:143], a[16:31]
	v_max_f32_e32 v128, v128, v130
	s_nop 0
	v_mov_b32_e32 v130, v128
	s_nop 1
	v_permlane32_swap_b32_e32 v128, v130
	v_max_f32_e32 v128, v128, v130
	v_max_f32_e32 v130, v129, v128
	v_mfma_f32_32x32x16_f16 a[32:47], v[60:63], v[52:55], a[32:47]
	v_cmp_lt_f32_e32 vcc, s79, v130
	s_cmp_lg_u64 vcc, 0
	s_cselect_b64 s[0:1], -1, 0
	s_cbranch_vccnz .LBB3_28
